# GEMM K-loops (7.11): loop-carried SALU block and exit compare moved in front of the loop-back barrier, into the last MFMA group's shadow (5 loops); on top of the attention no-copy version
# speedup vs baseline: 1.0037x; 1.0037x over previous
.LBB0_238:
	ds_read_b128 v[20:23], v203
	ds_read_b128 v[34:37], v203 offset:1024
	ds_read_b128 v[38:41], v203 offset:2048
	ds_read_b128 v[208:211], v203 offset:3072
	ds_read_b128 v[212:215], v207
	ds_read_b128 v[216:219], v207 offset:1024
	ds_read_b128 v[226:229], v207 offset:2048
	ds_read_b128 v[230:233], v207 offset:3072
	s_add_u32 s28, s10, 0xfffc0080
	s_addc_u32 s29, s11, -1
	s_cmp_eq_u32 s39, 12
	s_cselect_b32 s49, s2, s29
	s_cselect_b32 s48, s3, s28
	s_cselect_b32 s47, s13, s33
	s_cselect_b32 s46, s15, s20
	v_lshl_add_u64 v[24:25], s[10:11], 0, v[174:175]
	s_add_i32 m0, s58, 0xc000
	ds_read_b128 v[234:237], v224
	ds_read_b128 v[238:241], v224 offset:1024
	ds_read_b128 v[242:245], v224 offset:2048
	ds_read_b128 v[246:249], v224 offset:3072
	ds_read_b128 v[250:253], v224 offset:4096
	ds_read_b128 v[220:223], v224 offset:5120
	ds_read_b128 v[178:181], v224 offset:6144
	ds_read_b128 v[196:199], v224 offset:7168
	global_load_lds_dwordx4 v[24:25], off
	v_lshl_add_u64 v[24:25], s[10:11], 0, v[176:177]
	s_add_i32 m0, s58, 0xe000
	s_nop 0
	global_load_lds_dwordx4 v[24:25], off
	s_waitcnt vmcnt(8)
	s_waitcnt lgkmcnt(0)
	s_barrier
	s_setprio 1
	s_waitcnt lgkmcnt(0)
	v_mfma_i32_16x16x64_i8 v[142:145], v[20:23], v[234:237], v[142:145]
	v_mfma_i32_16x16x64_i8 v[138:141], v[38:41], v[234:237], v[138:141]
	v_mfma_i32_16x16x64_i8 v[126:129], v[20:23], v[242:245], v[126:129]
	v_mfma_i32_16x16x64_i8 v[122:125], v[38:41], v[242:245], v[122:125]
	v_mfma_i32_16x16x64_i8 v[110:113], v[20:23], v[250:253], v[110:113]
	v_mfma_i32_16x16x64_i8 v[106:109], v[38:41], v[250:253], v[106:109]
	v_mfma_i32_16x16x64_i8 v[94:97], v[20:23], v[178:181], v[94:97]
	v_mfma_i32_16x16x64_i8 v[90:93], v[38:41], v[178:181], v[90:93]
	v_mfma_i32_16x16x64_i8 v[142:145], v[34:37], v[238:241], v[142:145]
	v_mfma_i32_16x16x64_i8 v[138:141], v[208:211], v[238:241], v[138:141]
	v_mfma_i32_16x16x64_i8 v[126:129], v[34:37], v[246:249], v[126:129]
	v_mfma_i32_16x16x64_i8 v[122:125], v[208:211], v[246:249], v[122:125]
	v_mfma_i32_16x16x64_i8 v[110:113], v[34:37], v[220:223], v[110:113]
	v_mfma_i32_16x16x64_i8 v[106:109], v[208:211], v[220:223], v[106:109]
	v_mfma_i32_16x16x64_i8 v[94:97], v[34:37], v[196:199], v[94:97]
	v_mfma_i32_16x16x64_i8 v[90:93], v[208:211], v[196:199], v[90:93]
	s_setprio 0
	s_setprio 1
	v_mfma_i32_16x16x64_i8 v[134:137], v[212:215], v[234:237], v[134:137]
	v_mfma_i32_16x16x64_i8 v[130:133], v[226:229], v[234:237], v[130:133]
	v_mfma_i32_16x16x64_i8 v[118:121], v[212:215], v[242:245], v[118:121]
	v_mfma_i32_16x16x64_i8 v[114:117], v[226:229], v[242:245], v[114:117]
	v_mfma_i32_16x16x64_i8 v[102:105], v[212:215], v[250:253], v[102:105]
	v_mfma_i32_16x16x64_i8 v[98:101], v[226:229], v[250:253], v[98:101]
	v_mfma_i32_16x16x64_i8 v[86:89], v[212:215], v[178:181], v[86:89]
	v_mfma_i32_16x16x64_i8 v[82:85], v[226:229], v[178:181], v[82:85]
	v_mfma_i32_16x16x64_i8 v[134:137], v[216:219], v[238:241], v[134:137]
	v_mfma_i32_16x16x64_i8 v[130:133], v[230:233], v[238:241], v[130:133]
	v_mfma_i32_16x16x64_i8 v[118:121], v[216:219], v[246:249], v[118:121]
	v_mfma_i32_16x16x64_i8 v[114:117], v[230:233], v[246:249], v[114:117]
	v_mfma_i32_16x16x64_i8 v[102:105], v[216:219], v[220:223], v[102:105]
	v_mfma_i32_16x16x64_i8 v[98:101], v[230:233], v[220:223], v[98:101]
	v_mfma_i32_16x16x64_i8 v[86:89], v[216:219], v[196:199], v[86:89]
	v_mfma_i32_16x16x64_i8 v[82:85], v[230:233], v[196:199], v[82:85]
	s_setprio 0
	s_barrier
	s_add_i32 s28, s80, s57
	v_lshl_add_u64 v[184:185], s[46:47], 0, v[148:149]
	s_mov_b32 m0, s28
	ds_read_b128 v[178:181], v224 offset:16384
	ds_read_b128 v[196:199], v224 offset:17408
	ds_read_b128 v[220:223], v224 offset:18432
	ds_read_b128 v[234:237], v224 offset:19456
	ds_read_b128 v[238:241], v224 offset:20480
	ds_read_b128 v[242:245], v224 offset:21504
	ds_read_b128 v[246:249], v224 offset:22528
	ds_read_b128 v[250:253], v224 offset:23552
	global_load_lds_dwordx4 v[184:185], off
	s_add_i32 m0, s28, 0x2000
	s_add_u32 s28, s46, 0x40000
	v_lshl_add_u64 v[188:189], s[46:47], 0, v[152:153]
	s_addc_u32 s29, s47, 0
	s_add_i32 s41, s81, s57
	global_load_lds_dwordx4 v[188:189], off
	v_lshl_add_u64 v[24:25], s[28:29], 0, v[148:149]
	s_mov_b32 m0, s41
	v_lshl_add_u64 v[192:193], s[48:49], 0, v[146:147]
	global_load_lds_dwordx4 v[24:25], off
	v_lshl_add_u64 v[24:25], s[28:29], 0, v[152:153]
	s_add_i32 m0, s41, 0x2000
	v_lshl_add_u64 v[200:201], s[48:49], 0, v[150:151]
	global_load_lds_dwordx4 v[24:25], off
	s_mov_b32 m0, s58
	s_nop 0
	global_load_lds_dwordx4 v[192:193], off
	s_mov_b32 m0, s59
	s_nop 0
	global_load_lds_dwordx4 v[200:201], off
	s_waitcnt vmcnt(8)
	s_waitcnt lgkmcnt(0)
	s_barrier
	s_setprio 1
	s_waitcnt lgkmcnt(0)
	v_mfma_i32_16x16x64_i8 v[78:81], v[20:23], v[178:181], v[78:81]
	v_mfma_i32_16x16x64_i8 v[74:77], v[38:41], v[178:181], v[74:77]
	v_mfma_i32_16x16x64_i8 v[62:65], v[20:23], v[220:223], v[62:65]
	v_mfma_i32_16x16x64_i8 v[58:61], v[38:41], v[220:223], v[58:61]
	v_mfma_i32_16x16x64_i8 v[46:49], v[20:23], v[238:241], v[46:49]
	v_mfma_i32_16x16x64_i8 v[42:45], v[38:41], v[238:241], v[42:45]
	v_mfma_i32_16x16x64_i8 v[14:17], v[20:23], v[246:249], v[14:17]
	v_mfma_i32_16x16x64_i8 v[10:13], v[38:41], v[246:249], v[10:13]
	v_mfma_i32_16x16x64_i8 v[78:81], v[34:37], v[196:199], v[78:81]
	v_mfma_i32_16x16x64_i8 v[74:77], v[208:211], v[196:199], v[74:77]
	v_mfma_i32_16x16x64_i8 v[62:65], v[34:37], v[234:237], v[62:65]
	v_mfma_i32_16x16x64_i8 v[58:61], v[208:211], v[234:237], v[58:61]
	v_mfma_i32_16x16x64_i8 v[46:49], v[34:37], v[242:245], v[46:49]
	v_mfma_i32_16x16x64_i8 v[42:45], v[208:211], v[242:245], v[42:45]
	v_mfma_i32_16x16x64_i8 v[14:17], v[34:37], v[250:253], v[14:17]
	v_mfma_i32_16x16x64_i8 v[10:13], v[208:211], v[250:253], v[10:13]
	s_setprio 0
	s_setprio 1
	v_mfma_i32_16x16x64_i8 v[50:53], v[226:229], v[220:223], v[50:53]
	v_mfma_i32_16x16x64_i8 v[30:33], v[212:215], v[238:241], v[30:33]
	v_mfma_i32_16x16x64_i8 v[24:27], v[226:229], v[238:241], v[26:29]
	v_mfma_i32_16x16x64_i8 v[6:9], v[212:215], v[246:249], v[6:9]
	v_mfma_i32_16x16x64_i8 v[2:5], v[226:229], v[246:249], v[2:5]
	v_mfma_i32_16x16x64_i8 v[20:23], v[212:215], v[178:181], v[70:73]
	v_mfma_i32_16x16x64_i8 v[34:37], v[226:229], v[178:181], v[66:69]
	v_mfma_i32_16x16x64_i8 v[38:41], v[212:215], v[220:223], v[54:57]
	v_mfma_i32_16x16x64_i8 v[50:53], v[230:233], v[234:237], v[50:53]
	v_mfma_i32_16x16x64_i8 v[30:33], v[216:219], v[242:245], v[30:33]
	v_mfma_i32_16x16x64_i8 v[24:27], v[230:233], v[242:245], v[24:27]
	v_mfma_i32_16x16x64_i8 v[6:9], v[216:219], v[250:253], v[6:9]
	v_mfma_i32_16x16x64_i8 v[2:5], v[230:233], v[250:253], v[2:5]
	v_mfma_i32_16x16x64_i8 v[20:23], v[216:219], v[196:199], v[20:23]
	v_mfma_i32_16x16x64_i8 v[34:37], v[230:233], v[196:199], v[34:37]
	v_mfma_i32_16x16x64_i8 v[38:41], v[216:219], v[234:237], v[38:41]
	s_setprio 0
	s_barrier
	s_add_i32 s41, 0, 0x18000
	v_add_u32_e32 v28, s41, v183
	s_add_i32 s50, 0, 0x1c000
	ds_read_b128 v[54:57], v28
	ds_read_b128 v[66:69], v28 offset:1024
	ds_read_b128 v[70:73], v28 offset:2048
	ds_read_b128 v[178:181], v28 offset:3072
	v_add_u32_e32 v28, s50, v183
	ds_read_b128 v[196:199], v28
	ds_read_b128 v[208:211], v28 offset:1024
	ds_read_b128 v[212:215], v28 offset:2048
	ds_read_b128 v[216:219], v28 offset:3072
	s_add_u32 s28, s48, 0x40000
	s_addc_u32 s29, s49, 0
	s_mov_b32 m0, s60
	v_lshl_add_u64 v[28:29], s[28:29], 0, v[146:147]
	ds_read_b128 v[220:223], v224 offset:32768
	ds_read_b128 v[226:229], v224 offset:33792
	ds_read_b128 v[230:233], v224 offset:34816
	ds_read_b128 v[234:237], v224 offset:35840
	ds_read_b128 v[238:241], v224 offset:36864
	ds_read_b128 v[242:245], v224 offset:37888
	ds_read_b128 v[246:249], v224 offset:38912
	ds_read_b128 v[250:253], v224 offset:39936
	global_load_lds_dwordx4 v[28:29], off
	v_lshl_add_u64 v[28:29], s[28:29], 0, v[150:151]
	s_mov_b32 m0, s61
	s_nop 0
	global_load_lds_dwordx4 v[28:29], off
	s_waitcnt vmcnt(8)
	s_waitcnt lgkmcnt(0)
	s_barrier
	s_setprio 1
	s_waitcnt lgkmcnt(0)
	v_mfma_i32_16x16x64_i8 v[142:145], v[54:57], v[220:223], v[142:145]
	v_mfma_i32_16x16x64_i8 v[138:141], v[70:73], v[220:223], v[138:141]
	v_mfma_i32_16x16x64_i8 v[126:129], v[54:57], v[230:233], v[126:129]
	v_mfma_i32_16x16x64_i8 v[122:125], v[70:73], v[230:233], v[122:125]
	v_mfma_i32_16x16x64_i8 v[110:113], v[54:57], v[238:241], v[110:113]
	v_mfma_i32_16x16x64_i8 v[106:109], v[70:73], v[238:241], v[106:109]
	v_mfma_i32_16x16x64_i8 v[94:97], v[54:57], v[246:249], v[94:97]
	v_mfma_i32_16x16x64_i8 v[90:93], v[70:73], v[246:249], v[90:93]
	v_mfma_i32_16x16x64_i8 v[142:145], v[66:69], v[226:229], v[142:145]
	v_mfma_i32_16x16x64_i8 v[138:141], v[178:181], v[226:229], v[138:141]
	v_mfma_i32_16x16x64_i8 v[126:129], v[66:69], v[234:237], v[126:129]
	v_mfma_i32_16x16x64_i8 v[122:125], v[178:181], v[234:237], v[122:125]
	v_mfma_i32_16x16x64_i8 v[110:113], v[66:69], v[242:245], v[110:113]
	v_mfma_i32_16x16x64_i8 v[106:109], v[178:181], v[242:245], v[106:109]
	v_mfma_i32_16x16x64_i8 v[94:97], v[66:69], v[250:253], v[94:97]
	v_mfma_i32_16x16x64_i8 v[90:93], v[178:181], v[250:253], v[90:93]
	s_setprio 0
	s_setprio 1
	v_mfma_i32_16x16x64_i8 v[134:137], v[196:199], v[220:223], v[134:137]
	v_mfma_i32_16x16x64_i8 v[130:133], v[212:215], v[220:223], v[130:133]
	v_mfma_i32_16x16x64_i8 v[118:121], v[196:199], v[230:233], v[118:121]
	v_mfma_i32_16x16x64_i8 v[114:117], v[212:215], v[230:233], v[114:117]
	v_mfma_i32_16x16x64_i8 v[102:105], v[196:199], v[238:241], v[102:105]
	v_mfma_i32_16x16x64_i8 v[98:101], v[212:215], v[238:241], v[98:101]
	v_mfma_i32_16x16x64_i8 v[86:89], v[196:199], v[246:249], v[86:89]
	v_mfma_i32_16x16x64_i8 v[82:85], v[212:215], v[246:249], v[82:85]
	v_mfma_i32_16x16x64_i8 v[134:137], v[208:211], v[226:229], v[134:137]
	v_mfma_i32_16x16x64_i8 v[130:133], v[216:219], v[226:229], v[130:133]
	v_mfma_i32_16x16x64_i8 v[118:121], v[208:211], v[234:237], v[118:121]
	v_mfma_i32_16x16x64_i8 v[114:117], v[216:219], v[234:237], v[114:117]
	v_mfma_i32_16x16x64_i8 v[102:105], v[208:211], v[242:245], v[102:105]
	v_mfma_i32_16x16x64_i8 v[98:101], v[216:219], v[242:245], v[98:101]
	v_mfma_i32_16x16x64_i8 v[86:89], v[208:211], v[250:253], v[86:89]
	v_mfma_i32_16x16x64_i8 v[82:85], v[216:219], v[250:253], v[82:85]
	s_setprio 0
	s_barrier
	s_add_i32 s28, s41, s57
	v_lshl_add_u64 v[28:29], v[184:185], 0, s[24:25]
	s_mov_b32 m0, s28
	ds_read_b128 v[220:223], v224 offset:49152
	ds_read_b128 v[226:229], v224 offset:50176
	ds_read_b128 v[230:233], v224 offset:51200
	ds_read_b128 v[234:237], v224 offset:52224
	ds_read_b128 v[238:241], v224 offset:53248
	ds_read_b128 v[242:245], v224 offset:54272
	ds_read_b128 v[246:249], v224 offset:55296
	ds_read_b128 v[250:253], v224 offset:56320
	global_load_lds_dwordx4 v[28:29], off
	s_add_i32 m0, s28, 0x2000
	s_add_u32 s28, s46, 0x40080
	v_lshl_add_u64 v[28:29], v[188:189], 0, s[24:25]
	s_addc_u32 s29, s47, 0
	s_add_i32 s41, s50, s57
	global_load_lds_dwordx4 v[28:29], off
	v_lshl_add_u64 v[28:29], s[28:29], 0, v[148:149]
	s_mov_b32 m0, s41
	s_nop 0
	global_load_lds_dwordx4 v[28:29], off
	v_lshl_add_u64 v[28:29], s[28:29], 0, v[152:153]
	s_add_i32 m0, s41, 0x2000
	s_nop 0
	global_load_lds_dwordx4 v[28:29], off
	v_lshl_add_u64 v[28:29], v[192:193], 0, s[24:25]
	s_mov_b32 m0, s64
	s_nop 0
	global_load_lds_dwordx4 v[28:29], off
	v_lshl_add_u64 v[28:29], v[200:201], 0, s[24:25]
	s_mov_b32 m0, s65
	s_nop 0
	global_load_lds_dwordx4 v[28:29], off
	s_waitcnt vmcnt(8)
	s_waitcnt lgkmcnt(0)
	s_barrier
	s_setprio 1
	s_waitcnt lgkmcnt(0)
	v_mfma_i32_16x16x64_i8 v[78:81], v[54:57], v[220:223], v[78:81]
	v_mfma_i32_16x16x64_i8 v[74:77], v[70:73], v[220:223], v[74:77]
	v_mfma_i32_16x16x64_i8 v[62:65], v[54:57], v[230:233], v[62:65]
	v_mfma_i32_16x16x64_i8 v[58:61], v[70:73], v[230:233], v[58:61]
	v_mfma_i32_16x16x64_i8 v[46:49], v[54:57], v[238:241], v[46:49]
	v_mfma_i32_16x16x64_i8 v[42:45], v[70:73], v[238:241], v[42:45]
	v_mfma_i32_16x16x64_i8 v[14:17], v[54:57], v[246:249], v[14:17]
	v_mfma_i32_16x16x64_i8 v[10:13], v[70:73], v[246:249], v[10:13]
	v_mfma_i32_16x16x64_i8 v[78:81], v[66:69], v[226:229], v[78:81]
	v_mfma_i32_16x16x64_i8 v[74:77], v[178:181], v[226:229], v[74:77]
	v_mfma_i32_16x16x64_i8 v[62:65], v[66:69], v[234:237], v[62:65]
	v_mfma_i32_16x16x64_i8 v[58:61], v[178:181], v[234:237], v[58:61]
	v_mfma_i32_16x16x64_i8 v[46:49], v[66:69], v[242:245], v[46:49]
	v_mfma_i32_16x16x64_i8 v[42:45], v[178:181], v[242:245], v[42:45]
	v_mfma_i32_16x16x64_i8 v[14:17], v[66:69], v[250:253], v[14:17]
	v_mfma_i32_16x16x64_i8 v[10:13], v[178:181], v[250:253], v[10:13]
	s_setprio 0
	s_setprio 1
	v_mfma_i32_16x16x64_i8 v[20:23], v[196:199], v[220:223], v[20:23]
	s_add_i32 s39, s39, 2
	s_add_u32 s10, s10, 0x100
	s_addc_u32 s11, s11, 0
	s_add_u32 s20, s20, 0x100
	s_addc_u32 s33, s33, 0
	s_cmp_gt_u32 s39, 13
	v_mfma_i32_16x16x64_i8 v[70:73], v[208:211], v[226:229], v[20:23]
	v_mfma_i32_16x16x64_i8 v[20:23], v[212:215], v[220:223], v[34:37]
	v_mfma_i32_16x16x64_i8 v[66:69], v[216:219], v[226:229], v[20:23]
	v_mfma_i32_16x16x64_i8 v[20:23], v[196:199], v[230:233], v[38:41]
	v_mfma_i32_16x16x64_i8 v[54:57], v[208:211], v[234:237], v[20:23]
	v_mfma_i32_16x16x64_i8 v[20:23], v[212:215], v[230:233], v[50:53]
	v_mfma_i32_16x16x64_i8 v[50:53], v[216:219], v[234:237], v[20:23]
	v_mfma_i32_16x16x64_i8 v[20:23], v[196:199], v[238:241], v[30:33]
	v_mfma_i32_16x16x64_i8 v[30:33], v[208:211], v[242:245], v[20:23]
	v_mfma_i32_16x16x64_i8 v[20:23], v[212:215], v[238:241], v[24:27]
	v_mfma_i32_16x16x64_i8 v[6:9], v[196:199], v[246:249], v[6:9]
	v_mfma_i32_16x16x64_i8 v[2:5], v[212:215], v[246:249], v[2:5]
	v_mfma_i32_16x16x64_i8 v[26:29], v[216:219], v[242:245], v[20:23]
	v_mfma_i32_16x16x64_i8 v[6:9], v[208:211], v[250:253], v[6:9]
	v_mfma_i32_16x16x64_i8 v[2:5], v[216:219], v[250:253], v[2:5]
	s_setprio 0
	s_barrier
	s_cbranch_scc0 .LBB0_238
	s_and_b64 vcc, exec, s[26:27]
	s_cbranch_vccz .LBB0_241
	s_barrier

.LBB0_992:
	ds_read_b128 v[26:29], v199
	ds_read_b128 v[30:33], v199 offset:1024
	ds_read_b128 v[18:21], v199 offset:2048
	ds_read_b128 v[22:25], v199 offset:3072
	ds_read_b128 v[10:13], v200
	ds_read_b128 v[14:17], v200 offset:1024
	ds_read_b128 v[2:5], v200 offset:2048
	ds_read_b128 v[6:9], v200 offset:3072
	s_add_u32 s24, s22, 0xfffc0080
	s_addc_u32 s25, s23, -1
	s_cmp_eq_u32 s46, 12
	s_cselect_b32 s27, s15, s25
	s_cselect_b32 s26, s42, s24
	s_cselect_b32 s25, s13, s45
	s_cselect_b32 s24, s43, s44
	v_lshl_add_u64 v[218:219], s[22:23], 0, v[170:171]
	s_add_i32 m0, s21, 0xc000
	ds_read_b128 v[180:183], v201
	ds_read_b128 v[184:187], v201 offset:1024
	ds_read_b128 v[202:205], v201 offset:2048
	ds_read_b128 v[206:209], v201 offset:3072
	ds_read_b128 v[210:213], v201 offset:4096
	ds_read_b128 v[214:217], v201 offset:5120
	ds_read_b128 v[224:227], v201 offset:6144
	ds_read_b128 v[228:231], v201 offset:7168
	global_load_lds_dwordx4 v[218:219], off
	v_lshl_add_u64 v[218:219], s[22:23], 0, v[172:173]
	s_add_i32 m0, s21, 0xe000
	s_nop 0
	global_load_lds_dwordx4 v[218:219], off
	s_waitcnt vmcnt(8)
	s_waitcnt lgkmcnt(0)
	s_barrier
	s_setprio 1
	s_waitcnt lgkmcnt(0)
	v_mfma_f32_16x16x128_f8f6f4 v[158:161], v[26:33], v[180:187], v[158:161]
	v_mfma_f32_16x16x128_f8f6f4 v[154:157], v[18:25], v[180:187], v[154:157]
	v_mfma_f32_16x16x128_f8f6f4 v[142:145], v[26:33], v[202:209], v[142:145]
	v_mfma_f32_16x16x128_f8f6f4 v[138:141], v[18:25], v[202:209], v[138:141]
	v_mfma_f32_16x16x128_f8f6f4 v[126:129], v[26:33], v[210:217], v[126:129]
	v_mfma_f32_16x16x128_f8f6f4 v[122:125], v[18:25], v[210:217], v[122:125]
	v_mfma_f32_16x16x128_f8f6f4 v[110:113], v[26:33], v[224:231], v[110:113]
	v_mfma_f32_16x16x128_f8f6f4 v[106:109], v[18:25], v[224:231], v[106:109]
	s_setprio 0
	s_setprio 1
	v_mfma_f32_16x16x128_f8f6f4 v[150:153], v[10:17], v[180:187], v[150:153]
	v_mfma_f32_16x16x128_f8f6f4 v[146:149], v[2:9], v[180:187], v[146:149]
	v_mfma_f32_16x16x128_f8f6f4 v[134:137], v[10:17], v[202:209], v[134:137]
	v_mfma_f32_16x16x128_f8f6f4 v[130:133], v[2:9], v[202:209], v[130:133]
	v_mfma_f32_16x16x128_f8f6f4 v[118:121], v[10:17], v[210:217], v[118:121]
	v_mfma_f32_16x16x128_f8f6f4 v[114:117], v[2:9], v[210:217], v[114:117]
	v_mfma_f32_16x16x128_f8f6f4 v[102:105], v[10:17], v[224:231], v[102:105]
	v_mfma_f32_16x16x128_f8f6f4 v[98:101], v[2:9], v[224:231], v[98:101]
	s_setprio 0
	s_barrier
	s_add_i32 s47, s36, s3
	v_lshl_add_u64 v[180:181], s[24:25], 0, v[164:165]
	s_mov_b32 m0, s47
	ds_read_b128 v[202:205], v201 offset:16384
	ds_read_b128 v[206:209], v201 offset:17408
	ds_read_b128 v[210:213], v201 offset:18432
	ds_read_b128 v[214:217], v201 offset:19456
	ds_read_b128 v[224:227], v201 offset:20480
	ds_read_b128 v[228:231], v201 offset:21504
	ds_read_b128 v[232:235], v201 offset:22528
	ds_read_b128 v[236:239], v201 offset:23552
	global_load_lds_dwordx4 v[180:181], off
	s_add_i32 m0, s47, 0x2000
	s_add_u32 s48, s24, 0x40000
	v_lshl_add_u64 v[182:183], s[24:25], 0, v[168:169]
	s_addc_u32 s49, s25, 0
	s_add_i32 s47, s37, s3
	global_load_lds_dwordx4 v[182:183], off
	v_lshl_add_u64 v[184:185], s[48:49], 0, v[164:165]
	s_mov_b32 m0, s47
	v_lshl_add_u64 v[186:187], s[26:27], 0, v[166:167]
	global_load_lds_dwordx4 v[184:185], off
	v_lshl_add_u64 v[184:185], s[48:49], 0, v[168:169]
	s_add_i32 m0, s47, 0x2000
	s_nop 0
	global_load_lds_dwordx4 v[184:185], off
	v_lshl_add_u64 v[184:185], s[26:27], 0, v[162:163]
	s_mov_b32 m0, s21
	s_nop 0
	global_load_lds_dwordx4 v[184:185], off
	s_mov_b32 m0, s28
	s_nop 0
	global_load_lds_dwordx4 v[186:187], off
	s_waitcnt vmcnt(8)
	s_waitcnt lgkmcnt(0)
	s_barrier
	s_setprio 1
	s_waitcnt lgkmcnt(0)
	v_mfma_f32_16x16x128_f8f6f4 v[94:97], v[26:33], v[202:209], v[94:97]
	v_mfma_f32_16x16x128_f8f6f4 v[90:93], v[18:25], v[202:209], v[90:93]
	v_mfma_f32_16x16x128_f8f6f4 v[78:81], v[26:33], v[210:217], v[78:81]
	v_mfma_f32_16x16x128_f8f6f4 v[74:77], v[18:25], v[210:217], v[74:77]
	v_mfma_f32_16x16x128_f8f6f4 v[62:65], v[26:33], v[224:231], v[62:65]
	v_mfma_f32_16x16x128_f8f6f4 v[58:61], v[18:25], v[224:231], v[58:61]
	v_mfma_f32_16x16x128_f8f6f4 v[46:49], v[26:33], v[232:239], v[46:49]
	v_mfma_f32_16x16x128_f8f6f4 v[42:45], v[18:25], v[232:239], v[42:45]
	s_setprio 0
	s_setprio 1
	v_mfma_f32_16x16x128_f8f6f4 v[86:89], v[10:17], v[202:209], v[86:89]
	v_mfma_f32_16x16x128_f8f6f4 v[82:85], v[2:9], v[202:209], v[82:85]
	v_mfma_f32_16x16x128_f8f6f4 v[70:73], v[10:17], v[210:217], v[70:73]
	v_mfma_f32_16x16x128_f8f6f4 v[66:69], v[2:9], v[210:217], v[66:69]
	v_mfma_f32_16x16x128_f8f6f4 v[54:57], v[10:17], v[224:231], v[54:57]
	v_mfma_f32_16x16x128_f8f6f4 v[50:53], v[2:9], v[224:231], v[50:53]
	v_mfma_f32_16x16x128_f8f6f4 v[38:41], v[10:17], v[232:239], v[38:41]
	v_mfma_f32_16x16x128_f8f6f4 v[34:37], v[2:9], v[232:239], v[34:37]
	s_setprio 0
	s_barrier
	s_add_i32 s47, 0, 0x18000
	s_add_i32 s48, 0, 0x1c000
	v_add_u32_e32 v14, s47, v197
	v_add_u32_e32 v30, s48, v197
	ds_read_b128 v[2:5], v14
	ds_read_b128 v[6:9], v14 offset:1024
	ds_read_b128 v[10:13], v14 offset:2048
	ds_read_b128 v[14:17], v14 offset:3072
	ds_read_b128 v[18:21], v30
	ds_read_b128 v[22:25], v30 offset:1024
	ds_read_b128 v[26:29], v30 offset:2048
	ds_read_b128 v[30:33], v30 offset:3072
	s_add_u32 s26, s26, 0x40000
	s_addc_u32 s27, s27, 0
	s_mov_b32 m0, s29
	v_lshl_add_u64 v[218:219], s[26:27], 0, v[162:163]
	ds_read_b128 v[202:205], v201 offset:32768
	ds_read_b128 v[206:209], v201 offset:33792
	ds_read_b128 v[210:213], v201 offset:34816
	ds_read_b128 v[214:217], v201 offset:35840
	ds_read_b128 v[224:227], v201 offset:36864
	ds_read_b128 v[228:231], v201 offset:37888
	ds_read_b128 v[232:235], v201 offset:38912
	ds_read_b128 v[236:239], v201 offset:39936
	global_load_lds_dwordx4 v[218:219], off
	v_lshl_add_u64 v[218:219], s[26:27], 0, v[166:167]
	s_mov_b32 m0, s30
	s_nop 0
	global_load_lds_dwordx4 v[218:219], off
	s_waitcnt vmcnt(8)
	s_waitcnt lgkmcnt(0)
	s_barrier
	s_setprio 1
	s_waitcnt lgkmcnt(0)
	v_mfma_f32_16x16x128_f8f6f4 v[158:161], v[2:9], v[202:209], v[158:161]
	v_mfma_f32_16x16x128_f8f6f4 v[154:157], v[10:17], v[202:209], v[154:157]
	v_mfma_f32_16x16x128_f8f6f4 v[142:145], v[2:9], v[210:217], v[142:145]
	v_mfma_f32_16x16x128_f8f6f4 v[138:141], v[10:17], v[210:217], v[138:141]
	v_mfma_f32_16x16x128_f8f6f4 v[126:129], v[2:9], v[224:231], v[126:129]
	v_mfma_f32_16x16x128_f8f6f4 v[122:125], v[10:17], v[224:231], v[122:125]
	v_mfma_f32_16x16x128_f8f6f4 v[110:113], v[2:9], v[232:239], v[110:113]
	v_mfma_f32_16x16x128_f8f6f4 v[106:109], v[10:17], v[232:239], v[106:109]
	s_setprio 0
	s_setprio 1
	v_mfma_f32_16x16x128_f8f6f4 v[150:153], v[18:25], v[202:209], v[150:153]
	v_mfma_f32_16x16x128_f8f6f4 v[146:149], v[26:33], v[202:209], v[146:149]
	v_mfma_f32_16x16x128_f8f6f4 v[134:137], v[18:25], v[210:217], v[134:137]
	v_mfma_f32_16x16x128_f8f6f4 v[130:133], v[26:33], v[210:217], v[130:133]
	v_mfma_f32_16x16x128_f8f6f4 v[118:121], v[18:25], v[224:231], v[118:121]
	v_mfma_f32_16x16x128_f8f6f4 v[114:117], v[26:33], v[224:231], v[114:117]
	v_mfma_f32_16x16x128_f8f6f4 v[102:105], v[18:25], v[232:239], v[102:105]
	v_mfma_f32_16x16x128_f8f6f4 v[98:101], v[26:33], v[232:239], v[98:101]
	s_setprio 0
	s_barrier
	s_add_i32 s26, s47, s3
	v_lshl_add_u64 v[180:181], v[180:181], 0, s[8:9]
	s_mov_b32 m0, s26
	ds_read_b128 v[202:205], v201 offset:49152
	ds_read_b128 v[206:209], v201 offset:50176
	ds_read_b128 v[210:213], v201 offset:51200
	ds_read_b128 v[214:217], v201 offset:52224
	ds_read_b128 v[224:227], v201 offset:53248
	ds_read_b128 v[228:231], v201 offset:54272
	ds_read_b128 v[232:235], v201 offset:55296
	ds_read_b128 v[236:239], v201 offset:56320
	global_load_lds_dwordx4 v[180:181], off
	s_add_i32 m0, s26, 0x2000
	s_add_u32 s24, s24, 0x40080
	v_lshl_add_u64 v[180:181], v[182:183], 0, s[8:9]
	s_addc_u32 s25, s25, 0
	s_add_i32 s26, s48, s3
	global_load_lds_dwordx4 v[180:181], off
	v_lshl_add_u64 v[180:181], s[24:25], 0, v[164:165]
	s_mov_b32 m0, s26
	s_nop 0
	global_load_lds_dwordx4 v[180:181], off
	v_lshl_add_u64 v[180:181], s[24:25], 0, v[168:169]
	s_add_i32 m0, s26, 0x2000
	s_nop 0
	global_load_lds_dwordx4 v[180:181], off
	v_lshl_add_u64 v[180:181], v[184:185], 0, s[8:9]
	s_mov_b32 m0, s33
	s_nop 0
	global_load_lds_dwordx4 v[180:181], off
	v_lshl_add_u64 v[180:181], v[186:187], 0, s[8:9]
	s_mov_b32 m0, s34
	s_nop 0
	global_load_lds_dwordx4 v[180:181], off
	s_waitcnt vmcnt(8)
	s_waitcnt lgkmcnt(0)
	s_barrier
	s_setprio 1
	s_waitcnt lgkmcnt(0)
	v_mfma_f32_16x16x128_f8f6f4 v[94:97], v[2:9], v[202:209], v[94:97]
	v_mfma_f32_16x16x128_f8f6f4 v[90:93], v[10:17], v[202:209], v[90:93]
	v_mfma_f32_16x16x128_f8f6f4 v[78:81], v[2:9], v[210:217], v[78:81]
	v_mfma_f32_16x16x128_f8f6f4 v[74:77], v[10:17], v[210:217], v[74:77]
	v_mfma_f32_16x16x128_f8f6f4 v[62:65], v[2:9], v[224:231], v[62:65]
	v_mfma_f32_16x16x128_f8f6f4 v[58:61], v[10:17], v[224:231], v[58:61]
	v_mfma_f32_16x16x128_f8f6f4 v[46:49], v[2:9], v[232:239], v[46:49]
	v_mfma_f32_16x16x128_f8f6f4 v[42:45], v[10:17], v[232:239], v[42:45]
	s_setprio 0
	s_setprio 1
	v_mfma_f32_16x16x128_f8f6f4 v[86:89], v[18:25], v[202:209], v[86:89]
	s_add_i32 s46, s46, 2
	s_add_u32 s22, s22, 0x100
	s_addc_u32 s23, s23, 0
	s_add_u32 s44, s44, 0x100
	s_addc_u32 s45, s45, 0
	s_cmp_gt_u32 s46, 13
	v_mfma_f32_16x16x128_f8f6f4 v[82:85], v[26:33], v[202:209], v[82:85]
	v_mfma_f32_16x16x128_f8f6f4 v[70:73], v[18:25], v[210:217], v[70:73]
	v_mfma_f32_16x16x128_f8f6f4 v[66:69], v[26:33], v[210:217], v[66:69]
	v_mfma_f32_16x16x128_f8f6f4 v[54:57], v[18:25], v[224:231], v[54:57]
	v_mfma_f32_16x16x128_f8f6f4 v[50:53], v[26:33], v[224:231], v[50:53]
	v_mfma_f32_16x16x128_f8f6f4 v[38:41], v[18:25], v[232:239], v[38:41]
	v_mfma_f32_16x16x128_f8f6f4 v[34:37], v[26:33], v[232:239], v[34:37]
	s_setprio 0
	s_barrier
	s_cbranch_scc0 .LBB0_992
	s_and_b64 vcc, exec, s[10:11]
	s_cbranch_vccz .LBB0_995
	s_barrier

.LBB0_1016:
	ds_read_b128 v[26:29], v188
	ds_read_b128 v[30:33], v188 offset:1024
	ds_read_b128 v[18:21], v188 offset:2048
	ds_read_b128 v[22:25], v188 offset:3072
	ds_read_b128 v[10:13], v189
	ds_read_b128 v[14:17], v189 offset:1024
	ds_read_b128 v[2:5], v189 offset:2048
	ds_read_b128 v[6:9], v189 offset:3072
	s_add_u32 s20, s18, 0xfffc0080
	s_addc_u32 s21, s19, -1
	s_cmp_eq_u32 s47, 12
	s_cselect_b32 s23, s11, s21
	s_cselect_b32 s22, s43, s20
	s_cselect_b32 s21, s9, s46
	s_cselect_b32 s20, s44, s45
	v_lshl_add_u64 v[194:195], s[18:19], 0, v[170:171]
	s_add_i32 m0, s17, 0xc000
	ds_read_b128 v[180:183], v190
	ds_read_b128 v[184:187], v190 offset:1024
	ds_read_b128 v[198:201], v190 offset:2048
	ds_read_b128 v[202:205], v190 offset:3072
	ds_read_b128 v[206:209], v190 offset:4096
	ds_read_b128 v[210:213], v190 offset:5120
	ds_read_b128 v[224:227], v190 offset:6144
	ds_read_b128 v[228:231], v190 offset:7168
	global_load_lds_dwordx4 v[194:195], off
	v_lshl_add_u64 v[194:195], s[18:19], 0, v[172:173]
	s_add_i32 m0, s17, 0xe000
	s_nop 0
	global_load_lds_dwordx4 v[194:195], off
	s_waitcnt vmcnt(8)
	s_waitcnt lgkmcnt(0)
	s_barrier
	s_setprio 1
	s_waitcnt lgkmcnt(0)
	v_mfma_f32_16x16x128_f8f6f4 v[158:161], v[26:33], v[180:187], v[158:161]
	v_mfma_f32_16x16x128_f8f6f4 v[154:157], v[18:25], v[180:187], v[154:157]
	v_mfma_f32_16x16x128_f8f6f4 v[142:145], v[26:33], v[198:205], v[142:145]
	v_mfma_f32_16x16x128_f8f6f4 v[138:141], v[18:25], v[198:205], v[138:141]
	v_mfma_f32_16x16x128_f8f6f4 v[126:129], v[26:33], v[206:213], v[126:129]
	v_mfma_f32_16x16x128_f8f6f4 v[122:125], v[18:25], v[206:213], v[122:125]
	v_mfma_f32_16x16x128_f8f6f4 v[110:113], v[26:33], v[224:231], v[110:113]
	v_mfma_f32_16x16x128_f8f6f4 v[106:109], v[18:25], v[224:231], v[106:109]
	s_setprio 0
	s_setprio 1
	v_mfma_f32_16x16x128_f8f6f4 v[150:153], v[10:17], v[180:187], v[150:153]
	v_mfma_f32_16x16x128_f8f6f4 v[146:149], v[2:9], v[180:187], v[146:149]
	v_mfma_f32_16x16x128_f8f6f4 v[134:137], v[10:17], v[198:205], v[134:137]
	v_mfma_f32_16x16x128_f8f6f4 v[130:133], v[2:9], v[198:205], v[130:133]
	v_mfma_f32_16x16x128_f8f6f4 v[118:121], v[10:17], v[206:213], v[118:121]
	v_mfma_f32_16x16x128_f8f6f4 v[114:117], v[2:9], v[206:213], v[114:117]
	v_mfma_f32_16x16x128_f8f6f4 v[102:105], v[10:17], v[224:231], v[102:105]
	v_mfma_f32_16x16x128_f8f6f4 v[98:101], v[2:9], v[224:231], v[98:101]
	s_setprio 0
	s_barrier
	s_add_i32 s48, s38, s27
	v_lshl_add_u64 v[180:181], s[20:21], 0, v[164:165]
	s_mov_b32 m0, s48
	ds_read_b128 v[198:201], v190 offset:16384
	ds_read_b128 v[202:205], v190 offset:17408
	ds_read_b128 v[206:209], v190 offset:18432
	ds_read_b128 v[210:213], v190 offset:19456
	ds_read_b128 v[224:227], v190 offset:20480
	ds_read_b128 v[228:231], v190 offset:21504
	ds_read_b128 v[232:235], v190 offset:22528
	ds_read_b128 v[236:239], v190 offset:23552
	global_load_lds_dwordx4 v[180:181], off
	s_add_i32 m0, s48, 0x2000
	s_add_u32 s48, s20, 0x40000
	v_lshl_add_u64 v[182:183], s[20:21], 0, v[168:169]
	s_addc_u32 s49, s21, 0
	s_add_i32 s50, s39, s27
	global_load_lds_dwordx4 v[182:183], off
	v_lshl_add_u64 v[184:185], s[48:49], 0, v[164:165]
	s_mov_b32 m0, s50
	v_lshl_add_u64 v[186:187], s[22:23], 0, v[166:167]
	global_load_lds_dwordx4 v[184:185], off
	v_lshl_add_u64 v[184:185], s[48:49], 0, v[168:169]
	s_add_i32 m0, s50, 0x2000
	s_nop 0
	global_load_lds_dwordx4 v[184:185], off
	v_lshl_add_u64 v[184:185], s[22:23], 0, v[162:163]
	s_mov_b32 m0, s17
	s_nop 0
	global_load_lds_dwordx4 v[184:185], off
	s_mov_b32 m0, s28
	s_nop 0
	global_load_lds_dwordx4 v[186:187], off
	s_waitcnt vmcnt(8)
	s_waitcnt lgkmcnt(0)
	s_barrier
	s_setprio 1
	s_waitcnt lgkmcnt(0)
	v_mfma_f32_16x16x128_f8f6f4 v[94:97], v[26:33], v[198:205], v[94:97]
	v_mfma_f32_16x16x128_f8f6f4 v[90:93], v[18:25], v[198:205], v[90:93]
	v_mfma_f32_16x16x128_f8f6f4 v[78:81], v[26:33], v[206:213], v[78:81]
	v_mfma_f32_16x16x128_f8f6f4 v[74:77], v[18:25], v[206:213], v[74:77]
	v_mfma_f32_16x16x128_f8f6f4 v[62:65], v[26:33], v[224:231], v[62:65]
	v_mfma_f32_16x16x128_f8f6f4 v[58:61], v[18:25], v[224:231], v[58:61]
	v_mfma_f32_16x16x128_f8f6f4 v[46:49], v[26:33], v[232:239], v[46:49]
	v_mfma_f32_16x16x128_f8f6f4 v[42:45], v[18:25], v[232:239], v[42:45]
	s_setprio 0
	s_setprio 1
	v_mfma_f32_16x16x128_f8f6f4 v[86:89], v[10:17], v[198:205], v[86:89]
	v_mfma_f32_16x16x128_f8f6f4 v[82:85], v[2:9], v[198:205], v[82:85]
	v_mfma_f32_16x16x128_f8f6f4 v[70:73], v[10:17], v[206:213], v[70:73]
	v_mfma_f32_16x16x128_f8f6f4 v[66:69], v[2:9], v[206:213], v[66:69]
	v_mfma_f32_16x16x128_f8f6f4 v[54:57], v[10:17], v[224:231], v[54:57]
	v_mfma_f32_16x16x128_f8f6f4 v[50:53], v[2:9], v[224:231], v[50:53]
	v_mfma_f32_16x16x128_f8f6f4 v[38:41], v[10:17], v[232:239], v[38:41]
	v_mfma_f32_16x16x128_f8f6f4 v[34:37], v[2:9], v[232:239], v[34:37]
	s_setprio 0
	s_barrier
	s_add_i32 s48, 0, 0x18000
	s_add_i32 s49, 0, 0x1c000
	v_add_u32_e32 v14, s48, v193
	v_add_u32_e32 v30, s49, v193
	ds_read_b128 v[2:5], v14
	ds_read_b128 v[6:9], v14 offset:1024
	ds_read_b128 v[10:13], v14 offset:2048
	ds_read_b128 v[14:17], v14 offset:3072
	ds_read_b128 v[18:21], v30
	ds_read_b128 v[22:25], v30 offset:1024
	ds_read_b128 v[26:29], v30 offset:2048
	ds_read_b128 v[30:33], v30 offset:3072
	s_add_u32 s22, s22, 0x40000
	s_addc_u32 s23, s23, 0
	s_mov_b32 m0, s29
	v_lshl_add_u64 v[194:195], s[22:23], 0, v[162:163]
	ds_read_b128 v[198:201], v190 offset:32768
	ds_read_b128 v[202:205], v190 offset:33792
	ds_read_b128 v[206:209], v190 offset:34816
	ds_read_b128 v[210:213], v190 offset:35840
	ds_read_b128 v[224:227], v190 offset:36864
	ds_read_b128 v[228:231], v190 offset:37888
	ds_read_b128 v[232:235], v190 offset:38912
	ds_read_b128 v[236:239], v190 offset:39936
	global_load_lds_dwordx4 v[194:195], off
	v_lshl_add_u64 v[194:195], s[22:23], 0, v[166:167]
	s_mov_b32 m0, s30
	s_nop 0
	global_load_lds_dwordx4 v[194:195], off
	s_waitcnt vmcnt(8)
	s_waitcnt lgkmcnt(0)
	s_barrier
	s_setprio 1
	s_waitcnt lgkmcnt(0)
	v_mfma_f32_16x16x128_f8f6f4 v[158:161], v[2:9], v[198:205], v[158:161]
	v_mfma_f32_16x16x128_f8f6f4 v[154:157], v[10:17], v[198:205], v[154:157]
	v_mfma_f32_16x16x128_f8f6f4 v[142:145], v[2:9], v[206:213], v[142:145]
	v_mfma_f32_16x16x128_f8f6f4 v[138:141], v[10:17], v[206:213], v[138:141]
	v_mfma_f32_16x16x128_f8f6f4 v[126:129], v[2:9], v[224:231], v[126:129]
	v_mfma_f32_16x16x128_f8f6f4 v[122:125], v[10:17], v[224:231], v[122:125]
	v_mfma_f32_16x16x128_f8f6f4 v[110:113], v[2:9], v[232:239], v[110:113]
	v_mfma_f32_16x16x128_f8f6f4 v[106:109], v[10:17], v[232:239], v[106:109]
	s_setprio 0
	s_setprio 1
	v_mfma_f32_16x16x128_f8f6f4 v[150:153], v[18:25], v[198:205], v[150:153]
	v_mfma_f32_16x16x128_f8f6f4 v[146:149], v[26:33], v[198:205], v[146:149]
	v_mfma_f32_16x16x128_f8f6f4 v[134:137], v[18:25], v[206:213], v[134:137]
	v_mfma_f32_16x16x128_f8f6f4 v[130:133], v[26:33], v[206:213], v[130:133]
	v_mfma_f32_16x16x128_f8f6f4 v[118:121], v[18:25], v[224:231], v[118:121]
	v_mfma_f32_16x16x128_f8f6f4 v[114:117], v[26:33], v[224:231], v[114:117]
	v_mfma_f32_16x16x128_f8f6f4 v[102:105], v[18:25], v[232:239], v[102:105]
	v_mfma_f32_16x16x128_f8f6f4 v[98:101], v[26:33], v[232:239], v[98:101]
	s_setprio 0
	s_barrier
	s_add_i32 s22, s48, s27
	v_lshl_add_u64 v[180:181], v[180:181], 0, s[4:5]
	s_mov_b32 m0, s22
	ds_read_b128 v[198:201], v190 offset:49152
	ds_read_b128 v[202:205], v190 offset:50176
	ds_read_b128 v[206:209], v190 offset:51200
	ds_read_b128 v[210:213], v190 offset:52224
	ds_read_b128 v[224:227], v190 offset:53248
	ds_read_b128 v[228:231], v190 offset:54272
	ds_read_b128 v[232:235], v190 offset:55296
	ds_read_b128 v[236:239], v190 offset:56320
	global_load_lds_dwordx4 v[180:181], off
	s_add_i32 m0, s22, 0x2000
	s_add_u32 s20, s20, 0x40080
	v_lshl_add_u64 v[180:181], v[182:183], 0, s[4:5]
	s_addc_u32 s21, s21, 0
	s_add_i32 s22, s49, s27
	global_load_lds_dwordx4 v[180:181], off
	v_lshl_add_u64 v[180:181], s[20:21], 0, v[164:165]
	s_mov_b32 m0, s22
	s_nop 0
	global_load_lds_dwordx4 v[180:181], off
	v_lshl_add_u64 v[180:181], s[20:21], 0, v[168:169]
	s_add_i32 m0, s22, 0x2000
	s_nop 0
	global_load_lds_dwordx4 v[180:181], off
	v_lshl_add_u64 v[180:181], v[184:185], 0, s[4:5]
	s_mov_b32 m0, s34
	s_nop 0
	global_load_lds_dwordx4 v[180:181], off
	v_lshl_add_u64 v[180:181], v[186:187], 0, s[4:5]
	s_mov_b32 m0, s35
	s_nop 0
	global_load_lds_dwordx4 v[180:181], off
	s_waitcnt vmcnt(8)
	s_waitcnt lgkmcnt(0)
	s_barrier
	s_setprio 1
	s_waitcnt lgkmcnt(0)
	v_mfma_f32_16x16x128_f8f6f4 v[94:97], v[2:9], v[198:205], v[94:97]
	v_mfma_f32_16x16x128_f8f6f4 v[90:93], v[10:17], v[198:205], v[90:93]
	v_mfma_f32_16x16x128_f8f6f4 v[78:81], v[2:9], v[206:213], v[78:81]
	v_mfma_f32_16x16x128_f8f6f4 v[74:77], v[10:17], v[206:213], v[74:77]
	v_mfma_f32_16x16x128_f8f6f4 v[62:65], v[2:9], v[224:231], v[62:65]
	v_mfma_f32_16x16x128_f8f6f4 v[58:61], v[10:17], v[224:231], v[58:61]
	v_mfma_f32_16x16x128_f8f6f4 v[46:49], v[2:9], v[232:239], v[46:49]
	v_mfma_f32_16x16x128_f8f6f4 v[42:45], v[10:17], v[232:239], v[42:45]
	s_setprio 0
	s_setprio 1
	v_mfma_f32_16x16x128_f8f6f4 v[86:89], v[18:25], v[198:205], v[86:89]
	s_add_i32 s47, s47, 2
	s_add_u32 s18, s18, 0x100
	s_addc_u32 s19, s19, 0
	s_add_u32 s45, s45, 0x100
	s_addc_u32 s46, s46, 0
	s_cmp_gt_u32 s47, 13
	v_mfma_f32_16x16x128_f8f6f4 v[82:85], v[26:33], v[198:205], v[82:85]
	v_mfma_f32_16x16x128_f8f6f4 v[70:73], v[18:25], v[206:213], v[70:73]
	v_mfma_f32_16x16x128_f8f6f4 v[66:69], v[26:33], v[206:213], v[66:69]
	v_mfma_f32_16x16x128_f8f6f4 v[54:57], v[18:25], v[224:231], v[54:57]
	v_mfma_f32_16x16x128_f8f6f4 v[50:53], v[26:33], v[224:231], v[50:53]
	v_mfma_f32_16x16x128_f8f6f4 v[38:41], v[18:25], v[232:239], v[38:41]
	v_mfma_f32_16x16x128_f8f6f4 v[34:37], v[26:33], v[232:239], v[34:37]
	s_setprio 0
	s_barrier
	s_cbranch_scc0 .LBB0_1016
	s_and_b64 vcc, exec, s[6:7]
	s_cbranch_vccz .LBB0_1019
	s_barrier

.LBB0_1099:
	ds_read_b128 v[26:29], v228
	ds_read_b128 v[30:33], v228 offset:1024
	ds_read_b128 v[18:21], v228 offset:2048
	ds_read_b128 v[22:25], v228 offset:3072
	ds_read_b128 v[10:13], v229
	ds_read_b128 v[14:17], v229 offset:1024
	ds_read_b128 v[2:5], v229 offset:2048
	ds_read_b128 v[6:9], v229 offset:3072
	s_add_u32 s26, s8, 0xffb80080
	s_addc_u32 s27, s9, -1
	s_cmp_eq_u32 s50, 12
	s_cselect_b32 s29, s23, s27
	s_cselect_b32 s28, s22, s26
	s_cselect_b32 s27, s3, s49
	s_cselect_b32 s26, s21, s48
	v_lshl_add_u64 v[208:209], s[8:9], 0, v[188:189]
	s_add_i32 m0, s33, 0xc000
	ds_read_b128 v[162:165], v230
	ds_read_b128 v[166:169], v230 offset:1024
	ds_read_b128 v[170:173], v230 offset:2048
	ds_read_b128 v[174:177], v230 offset:3072
	ds_read_b128 v[192:195], v230 offset:4096
	ds_read_b128 v[196:199], v230 offset:5120
	ds_read_b128 v[200:203], v230 offset:6144
	ds_read_b128 v[204:207], v230 offset:7168
	global_load_lds_dwordx4 v[208:209], off
	v_lshl_add_u64 v[208:209], s[8:9], 0, v[190:191]
	s_add_i32 m0, s33, 0xe000
	s_nop 0
	global_load_lds_dwordx4 v[208:209], off
	s_waitcnt vmcnt(8)
	s_waitcnt lgkmcnt(0)
	s_barrier
	s_setprio 1
	s_waitcnt lgkmcnt(0)
	v_mfma_f32_16x16x128_f8f6f4 v[158:161], v[26:33], v[162:169], v[158:161]
	v_mfma_f32_16x16x128_f8f6f4 v[154:157], v[18:25], v[162:169], v[154:157]
	v_mfma_f32_16x16x128_f8f6f4 v[142:145], v[26:33], v[170:177], v[142:145]
	v_mfma_f32_16x16x128_f8f6f4 v[138:141], v[18:25], v[170:177], v[138:141]
	v_mfma_f32_16x16x128_f8f6f4 v[126:129], v[26:33], v[192:199], v[126:129]
	v_mfma_f32_16x16x128_f8f6f4 v[122:125], v[18:25], v[192:199], v[122:125]
	v_mfma_f32_16x16x128_f8f6f4 v[110:113], v[26:33], v[200:207], v[110:113]
	v_mfma_f32_16x16x128_f8f6f4 v[106:109], v[18:25], v[200:207], v[106:109]
	s_setprio 0
	s_setprio 1
	v_mfma_f32_16x16x128_f8f6f4 v[150:153], v[10:17], v[162:169], v[150:153]
	v_mfma_f32_16x16x128_f8f6f4 v[146:149], v[2:9], v[162:169], v[146:149]
	v_mfma_f32_16x16x128_f8f6f4 v[134:137], v[10:17], v[170:177], v[134:137]
	v_mfma_f32_16x16x128_f8f6f4 v[130:133], v[2:9], v[170:177], v[130:133]
	v_mfma_f32_16x16x128_f8f6f4 v[118:121], v[10:17], v[192:199], v[118:121]
	v_mfma_f32_16x16x128_f8f6f4 v[114:117], v[2:9], v[192:199], v[114:117]
	v_mfma_f32_16x16x128_f8f6f4 v[102:105], v[10:17], v[200:207], v[102:105]
	v_mfma_f32_16x16x128_f8f6f4 v[98:101], v[2:9], v[200:207], v[98:101]
	s_setprio 0
	s_barrier
	s_add_i32 s51, s44, s31
	v_lshl_add_u64 v[162:163], s[26:27], 0, v[182:183]
	s_mov_b32 m0, s51
	ds_read_b128 v[170:173], v230 offset:16384
	ds_read_b128 v[174:177], v230 offset:17408
	ds_read_b128 v[192:195], v230 offset:18432
	ds_read_b128 v[196:199], v230 offset:19456
	ds_read_b128 v[200:203], v230 offset:20480
	ds_read_b128 v[204:207], v230 offset:21504
	ds_read_b128 v[208:211], v230 offset:22528
	ds_read_b128 v[212:215], v230 offset:23552
	global_load_lds_dwordx4 v[162:163], off
	s_add_i32 m0, s51, 0x2000
	s_add_u32 s52, s26, 0x40000
	v_lshl_add_u64 v[164:165], s[26:27], 0, v[186:187]
	s_addc_u32 s53, s27, 0
	s_add_i32 s51, s45, s31
	global_load_lds_dwordx4 v[164:165], off
	v_lshl_add_u64 v[166:167], s[52:53], 0, v[182:183]
	s_mov_b32 m0, s51
	v_lshl_add_u64 v[168:169], s[28:29], 0, v[184:185]
	global_load_lds_dwordx4 v[166:167], off
	v_lshl_add_u64 v[166:167], s[52:53], 0, v[186:187]
	s_add_i32 m0, s51, 0x2000
	s_nop 0
	global_load_lds_dwordx4 v[166:167], off
	v_lshl_add_u64 v[166:167], s[28:29], 0, v[180:181]
	s_mov_b32 m0, s33
	s_nop 0
	global_load_lds_dwordx4 v[166:167], off
	s_mov_b32 m0, s34
	s_nop 0
	global_load_lds_dwordx4 v[168:169], off
	s_waitcnt vmcnt(8)
	s_waitcnt lgkmcnt(0)
	s_barrier
	s_setprio 1
	s_waitcnt lgkmcnt(0)
	v_mfma_f32_16x16x128_f8f6f4 v[94:97], v[26:33], v[170:177], v[94:97]
	v_mfma_f32_16x16x128_f8f6f4 v[90:93], v[18:25], v[170:177], v[90:93]
	v_mfma_f32_16x16x128_f8f6f4 v[78:81], v[26:33], v[192:199], v[78:81]
	v_mfma_f32_16x16x128_f8f6f4 v[74:77], v[18:25], v[192:199], v[74:77]
	v_mfma_f32_16x16x128_f8f6f4 v[62:65], v[26:33], v[200:207], v[62:65]
	v_mfma_f32_16x16x128_f8f6f4 v[58:61], v[18:25], v[200:207], v[58:61]
	v_mfma_f32_16x16x128_f8f6f4 v[46:49], v[26:33], v[208:215], v[46:49]
	v_mfma_f32_16x16x128_f8f6f4 v[42:45], v[18:25], v[208:215], v[42:45]
	s_setprio 0
	s_setprio 1
	v_mfma_f32_16x16x128_f8f6f4 v[86:89], v[10:17], v[170:177], v[86:89]
	v_mfma_f32_16x16x128_f8f6f4 v[82:85], v[2:9], v[170:177], v[82:85]
	v_mfma_f32_16x16x128_f8f6f4 v[70:73], v[10:17], v[192:199], v[70:73]
	v_mfma_f32_16x16x128_f8f6f4 v[66:69], v[2:9], v[192:199], v[66:69]
	v_mfma_f32_16x16x128_f8f6f4 v[54:57], v[10:17], v[200:207], v[54:57]
	v_mfma_f32_16x16x128_f8f6f4 v[50:53], v[2:9], v[200:207], v[50:53]
	v_mfma_f32_16x16x128_f8f6f4 v[38:41], v[10:17], v[208:215], v[38:41]
	v_mfma_f32_16x16x128_f8f6f4 v[34:37], v[2:9], v[208:215], v[34:37]
	s_setprio 0
	s_barrier
	s_add_i32 s51, 0, 0x18000
	s_add_i32 s52, 0, 0x1c000
	v_add_u32_e32 v14, s51, v225
	v_add_u32_e32 v30, s52, v225
	ds_read_b128 v[2:5], v14
	ds_read_b128 v[6:9], v14 offset:1024
	ds_read_b128 v[10:13], v14 offset:2048
	ds_read_b128 v[14:17], v14 offset:3072
	ds_read_b128 v[18:21], v30
	ds_read_b128 v[22:25], v30 offset:1024
	ds_read_b128 v[26:29], v30 offset:2048
	ds_read_b128 v[30:33], v30 offset:3072
	s_add_u32 s28, s28, 0x480000
	s_addc_u32 s29, s29, 0
	s_mov_b32 m0, s35
	v_lshl_add_u64 v[216:217], s[28:29], 0, v[180:181]
	ds_read_b128 v[170:173], v230 offset:32768
	ds_read_b128 v[174:177], v230 offset:33792
	ds_read_b128 v[192:195], v230 offset:34816
	ds_read_b128 v[196:199], v230 offset:35840
	ds_read_b128 v[200:203], v230 offset:36864
	ds_read_b128 v[204:207], v230 offset:37888
	ds_read_b128 v[208:211], v230 offset:38912
	ds_read_b128 v[212:215], v230 offset:39936
	global_load_lds_dwordx4 v[216:217], off
	v_lshl_add_u64 v[216:217], s[28:29], 0, v[184:185]
	s_mov_b32 m0, s36
	s_nop 0
	global_load_lds_dwordx4 v[216:217], off
	s_waitcnt vmcnt(8)
	s_waitcnt lgkmcnt(0)
	s_barrier
	s_setprio 1
	s_waitcnt lgkmcnt(0)
	v_mfma_f32_16x16x128_f8f6f4 v[158:161], v[2:9], v[170:177], v[158:161]
	v_mfma_f32_16x16x128_f8f6f4 v[154:157], v[10:17], v[170:177], v[154:157]
	v_mfma_f32_16x16x128_f8f6f4 v[142:145], v[2:9], v[192:199], v[142:145]
	v_mfma_f32_16x16x128_f8f6f4 v[138:141], v[10:17], v[192:199], v[138:141]
	v_mfma_f32_16x16x128_f8f6f4 v[126:129], v[2:9], v[200:207], v[126:129]
	v_mfma_f32_16x16x128_f8f6f4 v[122:125], v[10:17], v[200:207], v[122:125]
	v_mfma_f32_16x16x128_f8f6f4 v[110:113], v[2:9], v[208:215], v[110:113]
	v_mfma_f32_16x16x128_f8f6f4 v[106:109], v[10:17], v[208:215], v[106:109]
	s_setprio 0
	s_setprio 1
	v_mfma_f32_16x16x128_f8f6f4 v[150:153], v[18:25], v[170:177], v[150:153]
	v_mfma_f32_16x16x128_f8f6f4 v[146:149], v[26:33], v[170:177], v[146:149]
	v_mfma_f32_16x16x128_f8f6f4 v[134:137], v[18:25], v[192:199], v[134:137]
	v_mfma_f32_16x16x128_f8f6f4 v[130:133], v[26:33], v[192:199], v[130:133]
	v_mfma_f32_16x16x128_f8f6f4 v[118:121], v[18:25], v[200:207], v[118:121]
	v_mfma_f32_16x16x128_f8f6f4 v[114:117], v[26:33], v[200:207], v[114:117]
	v_mfma_f32_16x16x128_f8f6f4 v[102:105], v[18:25], v[208:215], v[102:105]
	v_mfma_f32_16x16x128_f8f6f4 v[98:101], v[26:33], v[208:215], v[98:101]
	s_setprio 0
	s_barrier
	s_add_i32 s28, s51, s31
	v_lshl_add_u64 v[162:163], v[162:163], 0, s[12:13]
	s_mov_b32 m0, s28
	ds_read_b128 v[170:173], v230 offset:49152
	ds_read_b128 v[174:177], v230 offset:50176
	ds_read_b128 v[192:195], v230 offset:51200
	ds_read_b128 v[196:199], v230 offset:52224
	ds_read_b128 v[200:203], v230 offset:53248
	ds_read_b128 v[204:207], v230 offset:54272
	ds_read_b128 v[208:211], v230 offset:55296
	ds_read_b128 v[212:215], v230 offset:56320
	global_load_lds_dwordx4 v[162:163], off
	s_add_i32 m0, s28, 0x2000
	s_add_u32 s26, s26, 0x40080
	v_lshl_add_u64 v[162:163], v[164:165], 0, s[12:13]
	s_addc_u32 s27, s27, 0
	s_add_i32 s28, s52, s31
	global_load_lds_dwordx4 v[162:163], off
	v_lshl_add_u64 v[162:163], s[26:27], 0, v[182:183]
	s_mov_b32 m0, s28
	s_nop 0
	global_load_lds_dwordx4 v[162:163], off
	v_lshl_add_u64 v[162:163], s[26:27], 0, v[186:187]
	s_add_i32 m0, s28, 0x2000
	s_nop 0
	global_load_lds_dwordx4 v[162:163], off
	v_lshl_add_u64 v[162:163], v[166:167], 0, s[12:13]
	s_mov_b32 m0, s40
	s_nop 0
	global_load_lds_dwordx4 v[162:163], off
	v_lshl_add_u64 v[162:163], v[168:169], 0, s[12:13]
	s_mov_b32 m0, s41
	s_nop 0
	global_load_lds_dwordx4 v[162:163], off
	s_waitcnt vmcnt(8)
	s_waitcnt lgkmcnt(0)
	s_barrier
	s_setprio 1
	s_waitcnt lgkmcnt(0)
	v_mfma_f32_16x16x128_f8f6f4 v[94:97], v[2:9], v[170:177], v[94:97]
	v_mfma_f32_16x16x128_f8f6f4 v[90:93], v[10:17], v[170:177], v[90:93]
	v_mfma_f32_16x16x128_f8f6f4 v[78:81], v[2:9], v[192:199], v[78:81]
	v_mfma_f32_16x16x128_f8f6f4 v[74:77], v[10:17], v[192:199], v[74:77]
	v_mfma_f32_16x16x128_f8f6f4 v[62:65], v[2:9], v[200:207], v[62:65]
	v_mfma_f32_16x16x128_f8f6f4 v[58:61], v[10:17], v[200:207], v[58:61]
	v_mfma_f32_16x16x128_f8f6f4 v[46:49], v[2:9], v[208:215], v[46:49]
	v_mfma_f32_16x16x128_f8f6f4 v[42:45], v[10:17], v[208:215], v[42:45]
	s_setprio 0
	s_setprio 1
	v_mfma_f32_16x16x128_f8f6f4 v[86:89], v[18:25], v[170:177], v[86:89]
	s_add_i32 s50, s50, 2
	s_add_u32 s8, s8, 0x100
	s_addc_u32 s9, s9, 0
	s_add_u32 s48, s48, 0x100
	s_addc_u32 s49, s49, 0
	s_cmp_gt_u32 s50, 13
	v_mfma_f32_16x16x128_f8f6f4 v[82:85], v[26:33], v[170:177], v[82:85]
	v_mfma_f32_16x16x128_f8f6f4 v[70:73], v[18:25], v[192:199], v[70:73]
	v_mfma_f32_16x16x128_f8f6f4 v[66:69], v[26:33], v[192:199], v[66:69]
	v_mfma_f32_16x16x128_f8f6f4 v[54:57], v[18:25], v[200:207], v[54:57]
	v_mfma_f32_16x16x128_f8f6f4 v[50:53], v[26:33], v[200:207], v[50:53]
	v_mfma_f32_16x16x128_f8f6f4 v[38:41], v[18:25], v[208:215], v[38:41]
	v_mfma_f32_16x16x128_f8f6f4 v[34:37], v[26:33], v[208:215], v[34:37]
	s_setprio 0
	s_barrier
	s_cbranch_scc0 .LBB0_1099
	s_and_b64 vcc, exec, s[14:15]
	s_cbranch_vccz .LBB0_1102
	s_barrier

.LBB0_1279:
	s_add_u32 s26, s96, s4
	s_addc_u32 s27, s97, s5
	s_add_u32 s67, s26, 0x26004100
	s_addc_u32 s68, s27, 0
	s_cmpk_eq_i32 s4, 0x700
	v_lshl_add_u64 v[2:3], v[186:187], 0, s[4:5]
	s_cselect_b64 vcc, -1, 0
	v_cndmask_b32_e32 v188, v2, v172, vcc
	v_add_u32_e32 v2, s52, v206
	v_add_u32_e32 v6, s53, v206
	v_cndmask_b32_e32 v189, v3, v173, vcc
	ds_read_b128 v[26:29], v2
	ds_read_b128 v[30:33], v2 offset:1024
	ds_read_b128 v[18:21], v2 offset:2048
	ds_read_b128 v[22:25], v2 offset:3072
	ds_read_b128 v[10:13], v6
	ds_read_b128 v[14:17], v6 offset:1024
	ds_read_b128 v[2:5], v6 offset:2048
	ds_read_b128 v[6:9], v6 offset:3072
	s_and_b64 s[26:27], vcc, exec
	s_cselect_b32 s27, s1, s68
	s_cselect_b32 s26, s0, s67
	v_cndmask_b32_e32 v164, v217, v169, vcc
	v_cndmask_b32_e32 v194, v174, v171, vcc
	v_cndmask_b32_e32 v177, v176, v213, vcc
	v_cndmask_b32_e32 v181, v180, v214, vcc
	s_mov_b32 m0, s54
	v_lshl_add_u64 v[190:191], v[184:185], 0, s[4:5]
	ds_read_b128 v[224:227], v209
	ds_read_b128 v[228:231], v209 offset:1024
	ds_read_b128 v[232:235], v209 offset:2048
	ds_read_b128 v[236:239], v209 offset:3072
	ds_read_b128 v[240:243], v209 offset:4096
	ds_read_b128 v[244:247], v209 offset:5120
	ds_read_b128 v[196:199], v209 offset:6144
	ds_read_b128 v[200:203], v209 offset:7168
	global_load_lds_dwordx4 v[190:191], off
	v_lshl_add_u64 v[190:191], v[182:183], 0, s[4:5]
	s_mov_b32 m0, s55
	s_nop 0
	global_load_lds_dwordx4 v[190:191], off
	s_waitcnt vmcnt(8)
	s_waitcnt lgkmcnt(0)
	s_barrier
	s_setprio 1
	s_waitcnt lgkmcnt(0)
	v_mfma_f32_16x16x128_f8f6f4 v[158:161], v[26:33], v[224:231], v[158:161]
	v_mfma_f32_16x16x128_f8f6f4 v[154:157], v[18:25], v[224:231], v[154:157]
	v_mfma_f32_16x16x128_f8f6f4 v[142:145], v[26:33], v[232:239], v[142:145]
	v_mfma_f32_16x16x128_f8f6f4 v[138:141], v[18:25], v[232:239], v[138:141]
	v_mfma_f32_16x16x128_f8f6f4 v[126:129], v[26:33], v[240:247], v[126:129]
	v_mfma_f32_16x16x128_f8f6f4 v[122:125], v[18:25], v[240:247], v[122:125]
	v_mfma_f32_16x16x128_f8f6f4 v[110:113], v[26:33], v[196:203], v[110:113]
	v_mfma_f32_16x16x128_f8f6f4 v[106:109], v[18:25], v[196:203], v[106:109]
	s_setprio 0
	s_setprio 1
	v_mfma_f32_16x16x128_f8f6f4 v[150:153], v[10:17], v[224:231], v[150:153]
	v_mfma_f32_16x16x128_f8f6f4 v[146:149], v[2:9], v[224:231], v[146:149]
	v_mfma_f32_16x16x128_f8f6f4 v[134:137], v[10:17], v[232:239], v[134:137]
	v_mfma_f32_16x16x128_f8f6f4 v[130:133], v[2:9], v[232:239], v[130:133]
	v_mfma_f32_16x16x128_f8f6f4 v[118:121], v[10:17], v[240:247], v[118:121]
	v_mfma_f32_16x16x128_f8f6f4 v[114:117], v[2:9], v[240:247], v[114:117]
	v_mfma_f32_16x16x128_f8f6f4 v[102:105], v[10:17], v[196:203], v[102:105]
	v_mfma_f32_16x16x128_f8f6f4 v[98:101], v[2:9], v[196:203], v[98:101]
	s_setprio 0
	s_barrier
	s_mov_b32 m0, s56
	v_lshl_add_u64 v[190:191], v[188:189], 0, v[166:167]
	ds_read_b128 v[224:227], v209 offset:16384
	ds_read_b128 v[228:231], v209 offset:17408
	ds_read_b128 v[232:235], v209 offset:18432
	ds_read_b128 v[236:239], v209 offset:19456
	ds_read_b128 v[240:243], v209 offset:20480
	ds_read_b128 v[244:247], v209 offset:21504
	ds_read_b128 v[198:201], v209 offset:22528
	ds_read_b128 v[202:205], v209 offset:23552
	global_load_lds_dwordx4 v[190:191], off
	v_lshl_add_u64 v[192:193], v[188:189], 0, v[162:163]
	s_mov_b32 m0, s57
	v_lshl_add_u64 v[196:197], v[188:189], 0, s[8:9]
	global_load_lds_dwordx4 v[192:193], off
	v_lshl_add_u64 v[220:221], v[196:197], 0, v[166:167]
	s_mov_b32 m0, s58
	v_lshl_add_u64 v[196:197], v[196:197], 0, v[162:163]
	global_load_lds_dwordx4 v[220:221], off
	s_mov_b32 m0, s59
	v_mov_b32_e32 v195, v165
	global_load_lds_dwordx4 v[196:197], off
	s_mov_b32 m0, s29
	v_lshl_add_u64 v[196:197], s[26:27], 0, v[164:165]
	global_load_lds_dwordx4 v164, s[26:27]
	s_mov_b32 m0, s30
	s_nop 0
	global_load_lds_dwordx4 v194, s[26:27]
	s_waitcnt vmcnt(8)
	s_waitcnt lgkmcnt(0)
	v_lshl_add_u64 v[194:195], s[26:27], 0, v[194:195]
	s_barrier
	s_setprio 1
	s_waitcnt lgkmcnt(0)
	v_mfma_f32_16x16x128_f8f6f4 v[94:97], v[26:33], v[224:231], v[94:97]
	v_mfma_f32_16x16x128_f8f6f4 v[90:93], v[18:25], v[224:231], v[90:93]
	v_mfma_f32_16x16x128_f8f6f4 v[78:81], v[26:33], v[232:239], v[78:81]
	v_mfma_f32_16x16x128_f8f6f4 v[74:77], v[18:25], v[232:239], v[74:77]
	v_mfma_f32_16x16x128_f8f6f4 v[54:57], v[26:33], v[240:247], v[54:57]
	v_mfma_f32_16x16x128_f8f6f4 v[50:53], v[18:25], v[240:247], v[50:53]
	v_mfma_f32_16x16x128_f8f6f4 v[38:41], v[26:33], v[198:205], v[38:41]
	v_mfma_f32_16x16x128_f8f6f4 v[34:37], v[18:25], v[198:205], v[34:37]
	s_setprio 0
	s_setprio 1
	v_mfma_f32_16x16x128_f8f6f4 v[86:89], v[10:17], v[224:231], v[86:89]
	v_mfma_f32_16x16x128_f8f6f4 v[82:85], v[2:9], v[224:231], v[82:85]
	v_mfma_f32_16x16x128_f8f6f4 v[70:73], v[10:17], v[232:239], v[70:73]
	v_mfma_f32_16x16x128_f8f6f4 v[66:69], v[2:9], v[232:239], v[66:69]
	v_mfma_f32_16x16x128_f8f6f4 v[62:65], v[10:17], v[240:247], v[62:65]
	v_mfma_f32_16x16x128_f8f6f4 v[58:61], v[2:9], v[240:247], v[58:61]
	v_mfma_f32_16x16x128_f8f6f4 v[46:49], v[10:17], v[198:205], v[46:49]
	v_mfma_f32_16x16x128_f8f6f4 v[42:45], v[2:9], v[198:205], v[42:45]
	s_setprio 0
	s_barrier
	v_add_u32_e32 v14, s60, v206
	v_add_u32_e32 v30, s61, v206
	ds_read_b128 v[2:5], v14
	ds_read_b128 v[6:9], v14 offset:1024
	ds_read_b128 v[10:13], v14 offset:2048
	ds_read_b128 v[14:17], v14 offset:3072
	ds_read_b128 v[18:21], v30
	ds_read_b128 v[22:25], v30 offset:1024
	ds_read_b128 v[26:29], v30 offset:2048
	ds_read_b128 v[30:33], v30 offset:3072
	s_mov_b32 m0, s31
	ds_read_b128 v[198:201], v209 offset:32768
	ds_read_b128 v[202:205], v209 offset:33792
	ds_read_b128 v[224:227], v209 offset:34816
	ds_read_b128 v[228:231], v209 offset:35840
	ds_read_b128 v[232:235], v209 offset:36864
	ds_read_b128 v[236:239], v209 offset:37888
	ds_read_b128 v[240:243], v209 offset:38912
	ds_read_b128 v[244:247], v209 offset:39936
	global_load_lds_dwordx4 v177, s[26:27]
	s_mov_b32 m0, s33
	s_nop 0
	global_load_lds_dwordx4 v181, s[26:27]
	s_waitcnt vmcnt(8)
	s_waitcnt lgkmcnt(0)
	s_barrier
	s_setprio 1
	s_waitcnt lgkmcnt(0)
	v_mfma_f32_16x16x128_f8f6f4 v[158:161], v[2:9], v[198:205], v[158:161]
	v_mfma_f32_16x16x128_f8f6f4 v[154:157], v[10:17], v[198:205], v[154:157]
	v_mfma_f32_16x16x128_f8f6f4 v[142:145], v[2:9], v[224:231], v[142:145]
	v_mfma_f32_16x16x128_f8f6f4 v[138:141], v[10:17], v[224:231], v[138:141]
	v_mfma_f32_16x16x128_f8f6f4 v[126:129], v[2:9], v[232:239], v[126:129]
	v_mfma_f32_16x16x128_f8f6f4 v[122:125], v[10:17], v[232:239], v[122:125]
	v_mfma_f32_16x16x128_f8f6f4 v[110:113], v[2:9], v[240:247], v[110:113]
	v_mfma_f32_16x16x128_f8f6f4 v[106:109], v[10:17], v[240:247], v[106:109]
	s_setprio 0
	s_setprio 1
	v_mfma_f32_16x16x128_f8f6f4 v[150:153], v[18:25], v[198:205], v[150:153]
	v_mfma_f32_16x16x128_f8f6f4 v[146:149], v[26:33], v[198:205], v[146:149]
	v_mfma_f32_16x16x128_f8f6f4 v[134:137], v[18:25], v[224:231], v[134:137]
	v_mfma_f32_16x16x128_f8f6f4 v[130:133], v[26:33], v[224:231], v[130:133]
	v_mfma_f32_16x16x128_f8f6f4 v[118:121], v[18:25], v[232:239], v[118:121]
	v_mfma_f32_16x16x128_f8f6f4 v[114:117], v[26:33], v[232:239], v[114:117]
	v_mfma_f32_16x16x128_f8f6f4 v[102:105], v[18:25], v[240:247], v[102:105]
	v_mfma_f32_16x16x128_f8f6f4 v[98:101], v[26:33], v[240:247], v[98:101]
	s_setprio 0
	s_barrier
	s_mov_b32 m0, s62
	v_lshl_add_u64 v[190:191], v[190:191], 0, s[18:19]
	ds_read_b128 v[198:201], v209 offset:49152
	ds_read_b128 v[202:205], v209 offset:50176
	ds_read_b128 v[224:227], v209 offset:51200
	ds_read_b128 v[228:231], v209 offset:52224
	ds_read_b128 v[232:235], v209 offset:53248
	ds_read_b128 v[236:239], v209 offset:54272
	ds_read_b128 v[240:243], v209 offset:55296
	ds_read_b128 v[244:247], v209 offset:56320
	global_load_lds_dwordx4 v[190:191], off
	v_lshl_add_u64 v[190:191], v[192:193], 0, s[18:19]
	s_mov_b32 m0, s63
	v_lshl_add_u64 v[188:189], v[188:189], 0, s[22:23]
	global_load_lds_dwordx4 v[190:191], off
	v_lshl_add_u64 v[190:191], v[188:189], 0, v[166:167]
	s_mov_b32 m0, s64
	v_lshl_add_u64 v[188:189], v[188:189], 0, v[162:163]
	global_load_lds_dwordx4 v[190:191], off
	s_mov_b32 m0, s65
	s_nop 0
	global_load_lds_dwordx4 v[188:189], off
	v_lshl_add_u64 v[188:189], v[196:197], 0, s[18:19]
	s_mov_b32 m0, s34
	s_nop 0
	global_load_lds_dwordx4 v[188:189], off
	v_lshl_add_u64 v[188:189], v[194:195], 0, s[18:19]
	s_mov_b32 m0, s35
	s_nop 0
	global_load_lds_dwordx4 v[188:189], off
	s_waitcnt vmcnt(8)
	s_waitcnt lgkmcnt(0)
	s_barrier
	s_setprio 1
	s_waitcnt lgkmcnt(0)
	v_mfma_f32_16x16x128_f8f6f4 v[94:97], v[2:9], v[198:205], v[94:97]
	v_mfma_f32_16x16x128_f8f6f4 v[90:93], v[10:17], v[198:205], v[90:93]
	v_mfma_f32_16x16x128_f8f6f4 v[78:81], v[2:9], v[224:231], v[78:81]
	v_mfma_f32_16x16x128_f8f6f4 v[74:77], v[10:17], v[224:231], v[74:77]
	v_mfma_f32_16x16x128_f8f6f4 v[54:57], v[2:9], v[232:239], v[54:57]
	v_mfma_f32_16x16x128_f8f6f4 v[50:53], v[10:17], v[232:239], v[50:53]
	v_mfma_f32_16x16x128_f8f6f4 v[38:41], v[2:9], v[240:247], v[38:41]
	v_mfma_f32_16x16x128_f8f6f4 v[34:37], v[10:17], v[240:247], v[34:37]
	s_setprio 0
	s_setprio 1
	v_mfma_f32_16x16x128_f8f6f4 v[86:89], v[18:25], v[198:205], v[86:89]
	s_add_i32 s66, s66, 2
	s_add_u32 s4, s4, 0x100
	s_addc_u32 s5, s5, 0
	s_cmp_gt_u32 s66, 13
	v_mfma_f32_16x16x128_f8f6f4 v[82:85], v[26:33], v[198:205], v[82:85]
	v_mfma_f32_16x16x128_f8f6f4 v[70:73], v[18:25], v[224:231], v[70:73]
	v_mfma_f32_16x16x128_f8f6f4 v[66:69], v[26:33], v[224:231], v[66:69]
	v_mfma_f32_16x16x128_f8f6f4 v[62:65], v[18:25], v[232:239], v[62:65]
	v_mfma_f32_16x16x128_f8f6f4 v[58:61], v[26:33], v[232:239], v[58:61]
	v_mfma_f32_16x16x128_f8f6f4 v[46:49], v[18:25], v[240:247], v[46:49]
	v_mfma_f32_16x16x128_f8f6f4 v[42:45], v[26:33], v[240:247], v[42:45]
	s_setprio 0
	s_barrier
	s_cbranch_scc0 .LBB0_1279
	s_and_b64 vcc, exec, s[24:25]
	s_cbranch_vccz .LBB0_1282
	s_barrier
